# speedup vs baseline: 1.0672x; 1.0672x over previous
.LBB1_4:
	v_add_u32_e32 v182, s19, v191
	v_add_u32_e32 v238, s19, v192
	ds_read_b128 v[178:181], v182 offset:32768
	ds_read_b128 v[194:197], v182 offset:34816
	ds_read_b128 v[198:201], v182 offset:36864
	ds_read_b128 v[202:205], v182 offset:38912
	ds_read_b128 v[206:209], v238
	ds_read_b128 v[210:213], v238 offset:2048
	ds_read_b128 v[214:217], v238 offset:4096
	ds_read_b128 v[218:221], v238 offset:6144
	ds_read_b128 v[222:225], v238 offset:8192
	ds_read_b128 v[226:229], v238 offset:10240
	ds_read_b128 v[230:233], v238 offset:12288
	ds_read_b128 v[234:237], v238 offset:14336
	s_min_u32 s21, s20, 29
	s_xor_b32 s19, s19, 0x10000
	v_add_u32_e32 v239, s19, v189
	s_waitcnt vmcnt(11)
	v_cvt_pk_bf16_f32 v13, v12, v13
	v_cvt_pk_bf16_f32 v12, v10, v11
	s_waitcnt vmcnt(10)
	v_cvt_pk_bf16_f32 v11, v20, v21
	v_cvt_pk_bf16_f32 v10, v18, v19
	ds_write2st64_b64 v239, v[12:13], v[10:11] offset1:8
	s_waitcnt vmcnt(9)
	v_cvt_pk_bf16_f32 v11, v24, v25
	v_cvt_pk_bf16_f32 v10, v22, v23
	s_waitcnt vmcnt(8)
	v_cvt_pk_bf16_f32 v13, v32, v33
	v_cvt_pk_bf16_f32 v12, v30, v31
	ds_write2st64_b64 v239, v[10:11], v[12:13] offset0:16 offset1:24
	s_waitcnt vmcnt(7)
	v_cvt_pk_bf16_f32 v11, v36, v37
	v_cvt_pk_bf16_f32 v10, v34, v35
	s_waitcnt vmcnt(6)
	v_cvt_pk_bf16_f32 v13, v40, v41
	v_cvt_pk_bf16_f32 v12, v38, v39
	ds_write2st64_b64 v239, v[10:11], v[12:13] offset0:32 offset1:40
	s_waitcnt vmcnt(5)
	v_cvt_pk_bf16_f32 v11, v44, v45
	v_cvt_pk_bf16_f32 v10, v42, v43
	s_waitcnt vmcnt(4)
	v_cvt_pk_bf16_f32 v13, v48, v49
	v_cvt_pk_bf16_f32 v12, v46, v47
	ds_write2st64_b64 v239, v[10:11], v[12:13] offset0:48 offset1:56
	s_waitcnt lgkmcnt(0)
	s_add_i32 s21, s21, 2
	s_barrier
	v_mfma_f32_16x16x32_bf16 v[174:177], v[178:181], v[206:209], v[174:177]
	s_lshl_b32 s22, s21, 1
	s_and_b32 s22, s22, 0x60
	s_add_i32 s22, s22, s12
	s_lshl_b32 s22, s22, 6
	v_mfma_f32_16x16x32_bf16 v[170:173], v[194:197], v[206:209], v[170:173]
	s_and_b32 s22, s22, 0x3f00
	s_or_b32 s22, s22, s13
	s_lshl_b32 s23, s21, 23
	s_lshl_b32 s22, s22, 9
	v_mfma_f32_16x16x32_bf16 v[158:161], v[198:201], v[206:209], v[158:161]
	s_and_b32 s23, s23, 0x7000000
	s_or_b32 s22, s22, s23
	s_lshl_b32 s23, s21, 8
	s_and_b32 s23, s23, 0x100
	s_or_b32 s22, s22, s23
	s_or_b32 s23, s22, 0x4000
	buffer_load_dwordx4 v[10:13], v1, s[4:7], s22 offen sc0 nt
	v_mfma_f32_16x16x32_bf16 v[142:145], v[202:205], v[206:209], v[142:145]
	v_mfma_f32_16x16x32_bf16 v[166:169], v[178:181], v[210:213], v[166:169]
	v_mfma_f32_16x16x32_bf16 v[162:165], v[194:197], v[210:213], v[162:165]
	v_mfma_f32_16x16x32_bf16 v[146:149], v[198:201], v[210:213], v[146:149]
	buffer_load_dwordx4 v[18:21], v1, s[4:7], s23 offen sc0 nt
	s_or_b32 s23, s22, 0x8000
	v_mfma_f32_16x16x32_bf16 v[122:125], v[202:205], v[210:213], v[122:125]
	v_mfma_f32_16x16x32_bf16 v[154:157], v[178:181], v[214:217], v[154:157]
	v_mfma_f32_16x16x32_bf16 v[150:153], v[194:197], v[214:217], v[150:153]
	v_mfma_f32_16x16x32_bf16 v[130:133], v[198:201], v[214:217], v[130:133]
	buffer_load_dwordx4 v[22:25], v1, s[4:7], s23 offen sc0 nt
	s_or_b32 s23, s22, 0xc000
	v_mfma_f32_16x16x32_bf16 v[106:109], v[202:205], v[214:217], v[106:109]
	v_mfma_f32_16x16x32_bf16 v[138:141], v[178:181], v[218:221], v[138:141]
	v_mfma_f32_16x16x32_bf16 v[134:137], v[194:197], v[218:221], v[134:137]
	v_mfma_f32_16x16x32_bf16 v[114:117], v[198:201], v[218:221], v[114:117]
	buffer_load_dwordx4 v[30:33], v1, s[4:7], s23 offen sc0 nt
	s_or_b32 s23, s22, 0x10000
	v_mfma_f32_16x16x32_bf16 v[90:93], v[202:205], v[218:221], v[90:93]
	v_mfma_f32_16x16x32_bf16 v[126:129], v[178:181], v[222:225], v[126:129]
	v_mfma_f32_16x16x32_bf16 v[118:121], v[194:197], v[222:225], v[118:121]
	v_mfma_f32_16x16x32_bf16 v[98:101], v[198:201], v[222:225], v[98:101]
	buffer_load_dwordx4 v[34:37], v1, s[4:7], s23 offen sc0 nt
	s_or_b32 s23, s22, 0x14000
	v_mfma_f32_16x16x32_bf16 v[74:77], v[202:205], v[222:225], v[74:77]
	v_mfma_f32_16x16x32_bf16 v[110:113], v[178:181], v[226:229], v[110:113]
	v_mfma_f32_16x16x32_bf16 v[102:105], v[194:197], v[226:229], v[102:105]
	v_mfma_f32_16x16x32_bf16 v[82:85], v[198:201], v[226:229], v[82:85]
	buffer_load_dwordx4 v[38:41], v1, s[4:7], s23 offen sc0 nt
	s_or_b32 s23, s22, 0x18000
	s_or_b32 s22, s22, 0x1c000
	v_mfma_f32_16x16x32_bf16 v[62:65], v[202:205], v[226:229], v[62:65]
	v_mfma_f32_16x16x32_bf16 v[94:97], v[178:181], v[230:233], v[94:97]
	v_mfma_f32_16x16x32_bf16 v[86:89], v[194:197], v[230:233], v[86:89]
	v_mfma_f32_16x16x32_bf16 v[70:73], v[198:201], v[230:233], v[70:73]
	buffer_load_dwordx4 v[42:45], v1, s[4:7], s23 offen sc0 nt
	v_mfma_f32_16x16x32_bf16 v[54:57], v[202:205], v[230:233], v[54:57]
	v_mfma_f32_16x16x32_bf16 v[78:81], v[178:181], v[234:237], v[78:81]
	v_mfma_f32_16x16x32_bf16 v[66:69], v[194:197], v[234:237], v[66:69]
	v_mfma_f32_16x16x32_bf16 v[58:61], v[198:201], v[234:237], v[58:61]
	buffer_load_dwordx4 v[46:49], v1, s[4:7], s22 offen sc0 nt
	v_mfma_f32_16x16x32_bf16 v[50:53], v[202:205], v[234:237], v[50:53]
	s_waitcnt lgkmcnt(0)
	s_barrier
	ds_read_b128 v[178:181], v182 offset:33792
	ds_read_b128 v[194:197], v182 offset:35840
	ds_read_b128 v[198:201], v182 offset:37888
	ds_read_b128 v[202:205], v182 offset:39936
	ds_read_b128 v[206:209], v238 offset:1024
	ds_read_b128 v[210:213], v238 offset:3072
	ds_read_b128 v[214:217], v238 offset:5120
	ds_read_b128 v[218:221], v238 offset:7168
	ds_read_b128 v[222:225], v238 offset:9216
	ds_read_b128 v[226:229], v238 offset:11264
	ds_read_b128 v[230:233], v238 offset:13312
	ds_read_b128 v[234:237], v238 offset:15360
	v_add_u32_e32 v182, s19, v190
	s_waitcnt vmcnt(11)
	ds_write_b128 v182, v[2:5] offset:32768
	s_waitcnt vmcnt(10)
	ds_write_b128 v182, v[6:9] offset:40960
	s_waitcnt vmcnt(9)
	ds_write_b128 v182, v[14:17] offset:49152
	s_waitcnt vmcnt(8)
	ds_write_b128 v182, v[26:29] offset:57344
	s_waitcnt lgkmcnt(0)
	s_barrier
	v_mfma_f32_16x16x32_bf16 v[174:177], v[178:181], v[206:209], v[174:177]
	s_lshl_b32 s21, s21, 7
	s_and_b32 s21, s21, 0x780
	s_or_b32 s21, s21, s14
	s_or_b32 s22, s21, 0x20000
	v_mfma_f32_16x16x32_bf16 v[170:173], v[194:197], v[206:209], v[170:173]
	v_mfma_f32_16x16x32_bf16 v[158:161], v[198:201], v[206:209], v[158:161]
	v_mfma_f32_16x16x32_bf16 v[142:145], v[202:205], v[206:209], v[142:145]
	v_mfma_f32_16x16x32_bf16 v[166:169], v[178:181], v[210:213], v[166:169]
	v_mfma_f32_16x16x32_bf16 v[162:165], v[194:197], v[210:213], v[162:165]
	buffer_load_dwordx4 v[2:5], v188, s[0:3], s21 offen sc1
	v_mfma_f32_16x16x32_bf16 v[146:149], v[198:201], v[210:213], v[146:149]
	v_mfma_f32_16x16x32_bf16 v[122:125], v[202:205], v[210:213], v[122:125]
	v_mfma_f32_16x16x32_bf16 v[154:157], v[178:181], v[214:217], v[154:157]
	v_mfma_f32_16x16x32_bf16 v[150:153], v[194:197], v[214:217], v[150:153]
	v_mfma_f32_16x16x32_bf16 v[130:133], v[198:201], v[214:217], v[130:133]
	v_mfma_f32_16x16x32_bf16 v[106:109], v[202:205], v[214:217], v[106:109]
	v_mfma_f32_16x16x32_bf16 v[138:141], v[178:181], v[218:221], v[138:141]
	v_mfma_f32_16x16x32_bf16 v[134:137], v[194:197], v[218:221], v[134:137]
	buffer_load_dwordx4 v[6:9], v188, s[0:3], s22 offen sc1
	s_or_b32 s22, s21, 0x40000
	s_or_b32 s21, s21, 0x60000
	v_mfma_f32_16x16x32_bf16 v[114:117], v[198:201], v[218:221], v[114:117]
	v_mfma_f32_16x16x32_bf16 v[90:93], v[202:205], v[218:221], v[90:93]
	v_mfma_f32_16x16x32_bf16 v[126:129], v[178:181], v[222:225], v[126:129]
	v_mfma_f32_16x16x32_bf16 v[118:121], v[194:197], v[222:225], v[118:121]
	v_mfma_f32_16x16x32_bf16 v[98:101], v[198:201], v[222:225], v[98:101]
	v_mfma_f32_16x16x32_bf16 v[74:77], v[202:205], v[222:225], v[74:77]
	v_mfma_f32_16x16x32_bf16 v[110:113], v[178:181], v[226:229], v[110:113]
	v_mfma_f32_16x16x32_bf16 v[102:105], v[194:197], v[226:229], v[102:105]
	buffer_load_dwordx4 v[14:17], v188, s[0:3], s22 offen sc1
	v_mfma_f32_16x16x32_bf16 v[82:85], v[198:201], v[226:229], v[82:85]
	v_mfma_f32_16x16x32_bf16 v[62:65], v[202:205], v[226:229], v[62:65]
	v_mfma_f32_16x16x32_bf16 v[94:97], v[178:181], v[230:233], v[94:97]
	v_mfma_f32_16x16x32_bf16 v[86:89], v[194:197], v[230:233], v[86:89]
	v_mfma_f32_16x16x32_bf16 v[70:73], v[198:201], v[230:233], v[70:73]
	v_mfma_f32_16x16x32_bf16 v[54:57], v[202:205], v[230:233], v[54:57]
	v_mfma_f32_16x16x32_bf16 v[78:81], v[178:181], v[234:237], v[78:81]
	v_mfma_f32_16x16x32_bf16 v[66:69], v[194:197], v[234:237], v[66:69]
	buffer_load_dwordx4 v[26:29], v188, s[0:3], s21 offen sc1
	v_mfma_f32_16x16x32_bf16 v[58:61], v[198:201], v[234:237], v[58:61]
	v_mfma_f32_16x16x32_bf16 v[50:53], v[202:205], v[234:237], v[50:53]
	s_and_b32 s21, s20, 15
	s_cmp_lg_u32 s21, 15
	s_cbranch_scc1 .LBB1_3
	s_and_b32 s21, s18, 32
	s_add_i32 s21, s21, s12
	s_lshl_b32 s21, s21, 6
	s_and_b32 s21, s21, 0x3f00
	v_add_lshl_u32 v182, v193, s21, 9
	v_lshl_add_u64 v[206:207], v[184:185], 0, v[182:183]
	v_add_co_u32_e32 v208, vcc, s8, v206
	s_nop 1
	v_addc_co_u32_e32 v209, vcc, 0, v207, vcc
	v_add_co_u32_e32 v210, vcc, s15, v206
	s_nop 1
	v_addc_co_u32_e32 v211, vcc, 0, v207, vcc
	v_add_co_u32_e32 v212, vcc, s9, v206
	s_nop 1
	v_addc_co_u32_e32 v213, vcc, 0, v207, vcc
	v_add_co_u32_e32 v214, vcc, s16, v206
	s_nop 1
	v_addc_co_u32_e32 v215, vcc, 0, v207, vcc
	v_add_co_u32_e32 v216, vcc, s10, v206
	s_nop 1
	v_addc_co_u32_e32 v217, vcc, 0, v207, vcc
	v_add_co_u32_e32 v218, vcc, s17, v206
	s_nop 1
	v_addc_co_u32_e32 v219, vcc, 0, v207, vcc
	v_add_co_u32_e32 v220, vcc, s11, v206
	s_nop 1
	v_addc_co_u32_e32 v221, vcc, 0, v207, vcc
	global_store_dwordx4 v[206:207], v[174:177], off
	global_store_dwordx4 v[206:207], v[170:173], off offset:64
	global_store_dwordx4 v[206:207], v[158:161], off offset:128
	global_store_dwordx4 v[206:207], v[142:145], off offset:192
	global_store_dwordx4 v[208:209], v[166:169], off
	global_store_dwordx4 v[208:209], v[162:165], off offset:64
	global_store_dwordx4 v[208:209], v[146:149], off offset:128
	global_store_dwordx4 v[208:209], v[122:125], off offset:192
	global_store_dwordx4 v[210:211], v[154:157], off
	global_store_dwordx4 v[210:211], v[150:153], off offset:64
	global_store_dwordx4 v[210:211], v[130:133], off offset:128
	global_store_dwordx4 v[210:211], v[106:109], off offset:192
	global_store_dwordx4 v[212:213], v[138:141], off
	global_store_dwordx4 v[212:213], v[134:137], off offset:64
	global_store_dwordx4 v[212:213], v[114:117], off offset:128
	global_store_dwordx4 v[212:213], v[90:93], off offset:192
	global_store_dwordx4 v[214:215], v[126:129], off
	global_store_dwordx4 v[214:215], v[118:121], off offset:64
	global_store_dwordx4 v[214:215], v[98:101], off offset:128
	global_store_dwordx4 v[214:215], v[74:77], off offset:192
	global_store_dwordx4 v[216:217], v[110:113], off
	global_store_dwordx4 v[216:217], v[102:105], off offset:64
	global_store_dwordx4 v[216:217], v[82:85], off offset:128
	global_store_dwordx4 v[216:217], v[62:65], off offset:192
	global_store_dwordx4 v[218:219], v[94:97], off
	global_store_dwordx4 v[218:219], v[86:89], off offset:64
	global_store_dwordx4 v[218:219], v[70:73], off offset:128
	global_store_dwordx4 v[218:219], v[54:57], off offset:192
	global_store_dwordx4 v[220:221], v[78:81], off
	global_store_dwordx4 v[220:221], v[66:69], off offset:64
	global_store_dwordx4 v[220:221], v[58:61], off offset:128
	global_store_dwordx4 v[220:221], v[50:53], off offset:192
.Lpd_tail:
	s_waitcnt lgkmcnt(0)
	s_barrier
	s_add_i32 s20, s20, 1
	s_add_i32 s18, s18, 2
	v_add_u32_e32 v182, s19, v191
	v_add_u32_e32 v238, s19, v192
	ds_read_b128 v[178:181], v182 offset:32768
	ds_read_b128 v[194:197], v182 offset:34816
	ds_read_b128 v[198:201], v182 offset:36864
	ds_read_b128 v[202:205], v182 offset:38912
	ds_read_b128 v[206:209], v238
	ds_read_b128 v[210:213], v238 offset:2048
	ds_read_b128 v[214:217], v238 offset:4096
	ds_read_b128 v[218:221], v238 offset:6144
	ds_read_b128 v[222:225], v238 offset:8192
	ds_read_b128 v[226:229], v238 offset:10240
	ds_read_b128 v[230:233], v238 offset:12288
	ds_read_b128 v[234:237], v238 offset:14336
	s_min_u32 s21, s20, 29
	s_xor_b32 s19, s19, 0x10000
	v_add_u32_e32 v239, s19, v189
	s_waitcnt vmcnt(43)
	v_cvt_pk_bf16_f32 v13, v12, v13
	v_cvt_pk_bf16_f32 v12, v10, v11
	s_waitcnt vmcnt(42)
	v_cvt_pk_bf16_f32 v11, v20, v21
	v_cvt_pk_bf16_f32 v10, v18, v19
	ds_write2st64_b64 v239, v[12:13], v[10:11] offset1:8
	s_waitcnt vmcnt(41)
	v_cvt_pk_bf16_f32 v11, v24, v25
	v_cvt_pk_bf16_f32 v10, v22, v23
	s_waitcnt vmcnt(40)
	v_cvt_pk_bf16_f32 v13, v32, v33
	v_cvt_pk_bf16_f32 v12, v30, v31
	ds_write2st64_b64 v239, v[10:11], v[12:13] offset0:16 offset1:24
	s_waitcnt vmcnt(39)
	v_cvt_pk_bf16_f32 v11, v36, v37
	v_cvt_pk_bf16_f32 v10, v34, v35
	s_waitcnt vmcnt(38)
	v_cvt_pk_bf16_f32 v13, v40, v41
	v_cvt_pk_bf16_f32 v12, v38, v39
	ds_write2st64_b64 v239, v[10:11], v[12:13] offset0:32 offset1:40
	s_waitcnt vmcnt(37)
	v_cvt_pk_bf16_f32 v11, v44, v45
	v_cvt_pk_bf16_f32 v10, v42, v43
	s_waitcnt vmcnt(36)
	v_cvt_pk_bf16_f32 v13, v48, v49
	v_cvt_pk_bf16_f32 v12, v46, v47
	ds_write2st64_b64 v239, v[10:11], v[12:13] offset0:48 offset1:56
	s_waitcnt lgkmcnt(0)
	s_add_i32 s21, s21, 2
	s_barrier
	v_mfma_f32_16x16x32_bf16 v[174:177], v[178:181], v[206:209], v[240:243]
	s_lshl_b32 s22, s21, 1
	s_and_b32 s22, s22, 0x60
	s_add_i32 s22, s22, s12
	s_lshl_b32 s22, s22, 6
	v_mfma_f32_16x16x32_bf16 v[170:173], v[194:197], v[206:209], v[244:247]
	s_and_b32 s22, s22, 0x3f00
	s_or_b32 s22, s22, s13
	s_lshl_b32 s23, s21, 23
	s_lshl_b32 s22, s22, 9
	v_mfma_f32_16x16x32_bf16 v[158:161], v[198:201], v[206:209], v[248:251]
	s_and_b32 s23, s23, 0x7000000
	s_or_b32 s22, s22, s23
	s_lshl_b32 s23, s21, 8
	s_and_b32 s23, s23, 0x100
	s_or_b32 s22, s22, s23
	s_or_b32 s23, s22, 0x4000
	buffer_load_dwordx4 v[10:13], v1, s[4:7], s22 offen sc0 nt
	v_mfma_f32_16x16x32_bf16 v[142:145], v[202:205], v[206:209], v[252:255]
	v_mfma_f32_16x16x32_bf16 v[166:169], v[178:181], v[210:213], v[240:243]
	v_mfma_f32_16x16x32_bf16 v[162:165], v[194:197], v[210:213], v[244:247]
	v_mfma_f32_16x16x32_bf16 v[146:149], v[198:201], v[210:213], v[248:251]
	buffer_load_dwordx4 v[18:21], v1, s[4:7], s23 offen sc0 nt
	s_or_b32 s23, s22, 0x8000
	v_mfma_f32_16x16x32_bf16 v[122:125], v[202:205], v[210:213], v[252:255]
	v_mfma_f32_16x16x32_bf16 v[154:157], v[178:181], v[214:217], v[240:243]
	v_mfma_f32_16x16x32_bf16 v[150:153], v[194:197], v[214:217], v[244:247]
	v_mfma_f32_16x16x32_bf16 v[130:133], v[198:201], v[214:217], v[248:251]
	buffer_load_dwordx4 v[22:25], v1, s[4:7], s23 offen sc0 nt
	s_or_b32 s23, s22, 0xc000
	v_mfma_f32_16x16x32_bf16 v[106:109], v[202:205], v[214:217], v[252:255]
	v_mfma_f32_16x16x32_bf16 v[138:141], v[178:181], v[218:221], v[240:243]
	v_mfma_f32_16x16x32_bf16 v[134:137], v[194:197], v[218:221], v[244:247]
	v_mfma_f32_16x16x32_bf16 v[114:117], v[198:201], v[218:221], v[248:251]
	buffer_load_dwordx4 v[30:33], v1, s[4:7], s23 offen sc0 nt
	s_or_b32 s23, s22, 0x10000
	v_mfma_f32_16x16x32_bf16 v[90:93], v[202:205], v[218:221], v[252:255]
	v_mfma_f32_16x16x32_bf16 v[126:129], v[178:181], v[222:225], v[240:243]
	v_mfma_f32_16x16x32_bf16 v[118:121], v[194:197], v[222:225], v[244:247]
	v_mfma_f32_16x16x32_bf16 v[98:101], v[198:201], v[222:225], v[248:251]
	buffer_load_dwordx4 v[34:37], v1, s[4:7], s23 offen sc0 nt
	s_or_b32 s23, s22, 0x14000
	v_mfma_f32_16x16x32_bf16 v[74:77], v[202:205], v[222:225], v[252:255]
	v_mfma_f32_16x16x32_bf16 v[110:113], v[178:181], v[226:229], v[240:243]
	v_mfma_f32_16x16x32_bf16 v[102:105], v[194:197], v[226:229], v[244:247]
	v_mfma_f32_16x16x32_bf16 v[82:85], v[198:201], v[226:229], v[248:251]
	buffer_load_dwordx4 v[38:41], v1, s[4:7], s23 offen sc0 nt
	s_or_b32 s23, s22, 0x18000
	s_or_b32 s22, s22, 0x1c000
	v_mfma_f32_16x16x32_bf16 v[62:65], v[202:205], v[226:229], v[252:255]
	v_mfma_f32_16x16x32_bf16 v[94:97], v[178:181], v[230:233], v[240:243]
	v_mfma_f32_16x16x32_bf16 v[86:89], v[194:197], v[230:233], v[244:247]
	v_mfma_f32_16x16x32_bf16 v[70:73], v[198:201], v[230:233], v[248:251]
	buffer_load_dwordx4 v[42:45], v1, s[4:7], s23 offen sc0 nt
	v_mfma_f32_16x16x32_bf16 v[54:57], v[202:205], v[230:233], v[252:255]
	v_mfma_f32_16x16x32_bf16 v[78:81], v[178:181], v[234:237], v[240:243]
	v_mfma_f32_16x16x32_bf16 v[66:69], v[194:197], v[234:237], v[244:247]
	v_mfma_f32_16x16x32_bf16 v[58:61], v[198:201], v[234:237], v[248:251]
	buffer_load_dwordx4 v[46:49], v1, s[4:7], s22 offen sc0 nt
	v_mfma_f32_16x16x32_bf16 v[50:53], v[202:205], v[234:237], v[252:255]
	s_waitcnt lgkmcnt(0)
	s_barrier
	ds_read_b128 v[178:181], v182 offset:33792
	ds_read_b128 v[194:197], v182 offset:35840
	ds_read_b128 v[198:201], v182 offset:37888
	ds_read_b128 v[202:205], v182 offset:39936
	ds_read_b128 v[206:209], v238 offset:1024
	ds_read_b128 v[210:213], v238 offset:3072
	ds_read_b128 v[214:217], v238 offset:5120
	ds_read_b128 v[218:221], v238 offset:7168
	ds_read_b128 v[222:225], v238 offset:9216
	ds_read_b128 v[226:229], v238 offset:11264
	ds_read_b128 v[230:233], v238 offset:13312
	ds_read_b128 v[234:237], v238 offset:15360
	v_add_u32_e32 v182, s19, v190
	s_waitcnt vmcnt(43)
	ds_write_b128 v182, v[2:5] offset:32768
	s_waitcnt vmcnt(42)
	ds_write_b128 v182, v[6:9] offset:40960
	s_waitcnt vmcnt(41)
	ds_write_b128 v182, v[14:17] offset:49152
	s_waitcnt vmcnt(40)
	ds_write_b128 v182, v[26:29] offset:57344
	s_waitcnt lgkmcnt(0)
	s_barrier
	v_mfma_f32_16x16x32_bf16 v[174:177], v[178:181], v[206:209], v[174:177]
	s_lshl_b32 s21, s21, 7
	s_and_b32 s21, s21, 0x780
	s_or_b32 s21, s21, s14
	s_or_b32 s22, s21, 0x20000
	v_mfma_f32_16x16x32_bf16 v[170:173], v[194:197], v[206:209], v[170:173]
	v_mfma_f32_16x16x32_bf16 v[158:161], v[198:201], v[206:209], v[158:161]
	v_mfma_f32_16x16x32_bf16 v[142:145], v[202:205], v[206:209], v[142:145]
	v_mfma_f32_16x16x32_bf16 v[166:169], v[178:181], v[210:213], v[166:169]
	v_mfma_f32_16x16x32_bf16 v[162:165], v[194:197], v[210:213], v[162:165]
	buffer_load_dwordx4 v[2:5], v188, s[0:3], s21 offen sc1
	v_mfma_f32_16x16x32_bf16 v[146:149], v[198:201], v[210:213], v[146:149]
	v_mfma_f32_16x16x32_bf16 v[122:125], v[202:205], v[210:213], v[122:125]
	v_mfma_f32_16x16x32_bf16 v[154:157], v[178:181], v[214:217], v[154:157]
	v_mfma_f32_16x16x32_bf16 v[150:153], v[194:197], v[214:217], v[150:153]
	v_mfma_f32_16x16x32_bf16 v[130:133], v[198:201], v[214:217], v[130:133]
	v_mfma_f32_16x16x32_bf16 v[106:109], v[202:205], v[214:217], v[106:109]
	v_mfma_f32_16x16x32_bf16 v[138:141], v[178:181], v[218:221], v[138:141]
	v_mfma_f32_16x16x32_bf16 v[134:137], v[194:197], v[218:221], v[134:137]
	buffer_load_dwordx4 v[6:9], v188, s[0:3], s22 offen sc1
	s_or_b32 s22, s21, 0x40000
	s_or_b32 s21, s21, 0x60000
	v_mfma_f32_16x16x32_bf16 v[114:117], v[198:201], v[218:221], v[114:117]
	v_mfma_f32_16x16x32_bf16 v[90:93], v[202:205], v[218:221], v[90:93]
	v_mfma_f32_16x16x32_bf16 v[126:129], v[178:181], v[222:225], v[126:129]
	v_mfma_f32_16x16x32_bf16 v[118:121], v[194:197], v[222:225], v[118:121]
	v_mfma_f32_16x16x32_bf16 v[98:101], v[198:201], v[222:225], v[98:101]
	v_mfma_f32_16x16x32_bf16 v[74:77], v[202:205], v[222:225], v[74:77]
	v_mfma_f32_16x16x32_bf16 v[110:113], v[178:181], v[226:229], v[110:113]
	v_mfma_f32_16x16x32_bf16 v[102:105], v[194:197], v[226:229], v[102:105]
	buffer_load_dwordx4 v[14:17], v188, s[0:3], s22 offen sc1
	v_mfma_f32_16x16x32_bf16 v[82:85], v[198:201], v[226:229], v[82:85]
	v_mfma_f32_16x16x32_bf16 v[62:65], v[202:205], v[226:229], v[62:65]
	v_mfma_f32_16x16x32_bf16 v[94:97], v[178:181], v[230:233], v[94:97]
	v_mfma_f32_16x16x32_bf16 v[86:89], v[194:197], v[230:233], v[86:89]
	v_mfma_f32_16x16x32_bf16 v[70:73], v[198:201], v[230:233], v[70:73]
	v_mfma_f32_16x16x32_bf16 v[54:57], v[202:205], v[230:233], v[54:57]
	v_mfma_f32_16x16x32_bf16 v[78:81], v[178:181], v[234:237], v[78:81]
	v_mfma_f32_16x16x32_bf16 v[66:69], v[194:197], v[234:237], v[66:69]
	buffer_load_dwordx4 v[26:29], v188, s[0:3], s21 offen sc1
	v_mfma_f32_16x16x32_bf16 v[58:61], v[198:201], v[234:237], v[58:61]
	v_mfma_f32_16x16x32_bf16 v[50:53], v[202:205], v[234:237], v[50:53]
	s_branch .LBB1_3
.Lt30:
	v_add_u32_e32 v182, s19, v191
	v_add_u32_e32 v238, s19, v192
	ds_read_b128 v[178:181], v182 offset:32768
	ds_read_b128 v[194:197], v182 offset:34816
	ds_read_b128 v[198:201], v182 offset:36864
	ds_read_b128 v[202:205], v182 offset:38912
	ds_read_b128 v[206:209], v238
	ds_read_b128 v[210:213], v238 offset:2048
	ds_read_b128 v[214:217], v238 offset:4096
	ds_read_b128 v[218:221], v238 offset:6144
	ds_read_b128 v[222:225], v238 offset:8192
	ds_read_b128 v[226:229], v238 offset:10240
	ds_read_b128 v[230:233], v238 offset:12288
	ds_read_b128 v[234:237], v238 offset:14336
	s_min_u32 s21, s20, 29
	s_xor_b32 s19, s19, 0x10000
	v_add_u32_e32 v239, s19, v189
	s_waitcnt vmcnt(11)
	v_cvt_pk_bf16_f32 v13, v12, v13
	v_cvt_pk_bf16_f32 v12, v10, v11
	s_waitcnt vmcnt(10)
	v_cvt_pk_bf16_f32 v11, v20, v21
	v_cvt_pk_bf16_f32 v10, v18, v19
	ds_write2st64_b64 v239, v[12:13], v[10:11] offset1:8
	s_waitcnt vmcnt(9)
	v_cvt_pk_bf16_f32 v11, v24, v25
	v_cvt_pk_bf16_f32 v10, v22, v23
	s_waitcnt vmcnt(8)
	v_cvt_pk_bf16_f32 v13, v32, v33
	v_cvt_pk_bf16_f32 v12, v30, v31
	ds_write2st64_b64 v239, v[10:11], v[12:13] offset0:16 offset1:24
	s_waitcnt vmcnt(7)
	v_cvt_pk_bf16_f32 v11, v36, v37
	v_cvt_pk_bf16_f32 v10, v34, v35
	s_waitcnt vmcnt(6)
	v_cvt_pk_bf16_f32 v13, v40, v41
	v_cvt_pk_bf16_f32 v12, v38, v39
	ds_write2st64_b64 v239, v[10:11], v[12:13] offset0:32 offset1:40
	s_waitcnt vmcnt(5)
	v_cvt_pk_bf16_f32 v11, v44, v45
	v_cvt_pk_bf16_f32 v10, v42, v43
	s_waitcnt vmcnt(4)
	v_cvt_pk_bf16_f32 v13, v48, v49
	v_cvt_pk_bf16_f32 v12, v46, v47
	ds_write2st64_b64 v239, v[10:11], v[12:13] offset0:48 offset1:56
	s_waitcnt lgkmcnt(0)
	s_add_i32 s21, s21, 2
	s_barrier
	v_mfma_f32_16x16x32_bf16 v[174:177], v[178:181], v[206:209], v[174:177]
	s_lshl_b32 s22, s21, 1
	s_and_b32 s22, s22, 0x60
	s_add_i32 s22, s22, s12
	s_lshl_b32 s22, s22, 6
	v_mfma_f32_16x16x32_bf16 v[170:173], v[194:197], v[206:209], v[170:173]
	s_and_b32 s22, s22, 0x3f00
	s_or_b32 s22, s22, s13
	s_lshl_b32 s23, s21, 23
	s_lshl_b32 s22, s22, 9
	v_mfma_f32_16x16x32_bf16 v[158:161], v[198:201], v[206:209], v[158:161]
	s_and_b32 s23, s23, 0x7000000
	s_or_b32 s22, s22, s23
	s_lshl_b32 s23, s21, 8
	s_and_b32 s23, s23, 0x100
	s_or_b32 s22, s22, s23
	s_or_b32 s23, s22, 0x4000
	v_mfma_f32_16x16x32_bf16 v[142:145], v[202:205], v[206:209], v[142:145]
	v_mfma_f32_16x16x32_bf16 v[166:169], v[178:181], v[210:213], v[166:169]
	v_mfma_f32_16x16x32_bf16 v[162:165], v[194:197], v[210:213], v[162:165]
	v_mfma_f32_16x16x32_bf16 v[146:149], v[198:201], v[210:213], v[146:149]
	s_or_b32 s23, s22, 0x8000
	v_mfma_f32_16x16x32_bf16 v[122:125], v[202:205], v[210:213], v[122:125]
	v_mfma_f32_16x16x32_bf16 v[154:157], v[178:181], v[214:217], v[154:157]
	v_mfma_f32_16x16x32_bf16 v[150:153], v[194:197], v[214:217], v[150:153]
	v_mfma_f32_16x16x32_bf16 v[130:133], v[198:201], v[214:217], v[130:133]
	s_or_b32 s23, s22, 0xc000
	v_mfma_f32_16x16x32_bf16 v[106:109], v[202:205], v[214:217], v[106:109]
	v_mfma_f32_16x16x32_bf16 v[138:141], v[178:181], v[218:221], v[138:141]
	v_mfma_f32_16x16x32_bf16 v[134:137], v[194:197], v[218:221], v[134:137]
	v_mfma_f32_16x16x32_bf16 v[114:117], v[198:201], v[218:221], v[114:117]
	s_or_b32 s23, s22, 0x10000
	v_mfma_f32_16x16x32_bf16 v[90:93], v[202:205], v[218:221], v[90:93]
	v_mfma_f32_16x16x32_bf16 v[126:129], v[178:181], v[222:225], v[126:129]
	v_mfma_f32_16x16x32_bf16 v[118:121], v[194:197], v[222:225], v[118:121]
	v_mfma_f32_16x16x32_bf16 v[98:101], v[198:201], v[222:225], v[98:101]
	s_or_b32 s23, s22, 0x14000
	v_mfma_f32_16x16x32_bf16 v[74:77], v[202:205], v[222:225], v[74:77]
	v_mfma_f32_16x16x32_bf16 v[110:113], v[178:181], v[226:229], v[110:113]
	v_mfma_f32_16x16x32_bf16 v[102:105], v[194:197], v[226:229], v[102:105]
	v_mfma_f32_16x16x32_bf16 v[82:85], v[198:201], v[226:229], v[82:85]
	s_or_b32 s23, s22, 0x18000
	s_or_b32 s22, s22, 0x1c000
	v_mfma_f32_16x16x32_bf16 v[62:65], v[202:205], v[226:229], v[62:65]
	v_mfma_f32_16x16x32_bf16 v[94:97], v[178:181], v[230:233], v[94:97]
	v_mfma_f32_16x16x32_bf16 v[86:89], v[194:197], v[230:233], v[86:89]
	v_mfma_f32_16x16x32_bf16 v[70:73], v[198:201], v[230:233], v[70:73]
	v_mfma_f32_16x16x32_bf16 v[54:57], v[202:205], v[230:233], v[54:57]
	v_mfma_f32_16x16x32_bf16 v[78:81], v[178:181], v[234:237], v[78:81]
	v_mfma_f32_16x16x32_bf16 v[66:69], v[194:197], v[234:237], v[66:69]
	v_mfma_f32_16x16x32_bf16 v[58:61], v[198:201], v[234:237], v[58:61]
	v_mfma_f32_16x16x32_bf16 v[50:53], v[202:205], v[234:237], v[50:53]
	s_waitcnt lgkmcnt(0)
	s_barrier
	ds_read_b128 v[178:181], v182 offset:33792
	ds_read_b128 v[194:197], v182 offset:35840
	ds_read_b128 v[198:201], v182 offset:37888
	ds_read_b128 v[202:205], v182 offset:39936
	ds_read_b128 v[206:209], v238 offset:1024
	ds_read_b128 v[210:213], v238 offset:3072
	ds_read_b128 v[214:217], v238 offset:5120
	ds_read_b128 v[218:221], v238 offset:7168
	ds_read_b128 v[222:225], v238 offset:9216
	ds_read_b128 v[226:229], v238 offset:11264
	ds_read_b128 v[230:233], v238 offset:13312
	ds_read_b128 v[234:237], v238 offset:15360
	v_add_u32_e32 v182, s19, v190
	s_waitcnt vmcnt(3)
	ds_write_b128 v182, v[2:5] offset:32768
	s_waitcnt vmcnt(2)
	ds_write_b128 v182, v[6:9] offset:40960
	s_waitcnt vmcnt(1)
	ds_write_b128 v182, v[14:17] offset:49152
	s_waitcnt vmcnt(0)
	ds_write_b128 v182, v[26:29] offset:57344
	s_waitcnt lgkmcnt(0)
	s_barrier
	v_mfma_f32_16x16x32_bf16 v[174:177], v[178:181], v[206:209], v[174:177]
	s_lshl_b32 s21, s21, 7
	s_and_b32 s21, s21, 0x780
	s_or_b32 s21, s21, s14
	s_or_b32 s22, s21, 0x20000
	v_mfma_f32_16x16x32_bf16 v[170:173], v[194:197], v[206:209], v[170:173]
	v_mfma_f32_16x16x32_bf16 v[158:161], v[198:201], v[206:209], v[158:161]
	v_mfma_f32_16x16x32_bf16 v[142:145], v[202:205], v[206:209], v[142:145]
	v_mfma_f32_16x16x32_bf16 v[166:169], v[178:181], v[210:213], v[166:169]
	v_mfma_f32_16x16x32_bf16 v[162:165], v[194:197], v[210:213], v[162:165]
	v_mfma_f32_16x16x32_bf16 v[146:149], v[198:201], v[210:213], v[146:149]
	v_mfma_f32_16x16x32_bf16 v[122:125], v[202:205], v[210:213], v[122:125]
	v_mfma_f32_16x16x32_bf16 v[154:157], v[178:181], v[214:217], v[154:157]
	v_mfma_f32_16x16x32_bf16 v[150:153], v[194:197], v[214:217], v[150:153]
	v_mfma_f32_16x16x32_bf16 v[130:133], v[198:201], v[214:217], v[130:133]
	v_mfma_f32_16x16x32_bf16 v[106:109], v[202:205], v[214:217], v[106:109]
	v_mfma_f32_16x16x32_bf16 v[138:141], v[178:181], v[218:221], v[138:141]
	v_mfma_f32_16x16x32_bf16 v[134:137], v[194:197], v[218:221], v[134:137]
	s_or_b32 s22, s21, 0x40000
	s_or_b32 s21, s21, 0x60000
	v_mfma_f32_16x16x32_bf16 v[114:117], v[198:201], v[218:221], v[114:117]
	v_mfma_f32_16x16x32_bf16 v[90:93], v[202:205], v[218:221], v[90:93]
	v_mfma_f32_16x16x32_bf16 v[126:129], v[178:181], v[222:225], v[126:129]
	v_mfma_f32_16x16x32_bf16 v[118:121], v[194:197], v[222:225], v[118:121]
	v_mfma_f32_16x16x32_bf16 v[98:101], v[198:201], v[222:225], v[98:101]
	v_mfma_f32_16x16x32_bf16 v[74:77], v[202:205], v[222:225], v[74:77]
	v_mfma_f32_16x16x32_bf16 v[110:113], v[178:181], v[226:229], v[110:113]
	v_mfma_f32_16x16x32_bf16 v[102:105], v[194:197], v[226:229], v[102:105]
	v_mfma_f32_16x16x32_bf16 v[82:85], v[198:201], v[226:229], v[82:85]
	v_mfma_f32_16x16x32_bf16 v[62:65], v[202:205], v[226:229], v[62:65]
	v_mfma_f32_16x16x32_bf16 v[94:97], v[178:181], v[230:233], v[94:97]
	v_mfma_f32_16x16x32_bf16 v[86:89], v[194:197], v[230:233], v[86:89]
	v_mfma_f32_16x16x32_bf16 v[70:73], v[198:201], v[230:233], v[70:73]
	v_mfma_f32_16x16x32_bf16 v[54:57], v[202:205], v[230:233], v[54:57]
	v_mfma_f32_16x16x32_bf16 v[78:81], v[178:181], v[234:237], v[78:81]
	v_mfma_f32_16x16x32_bf16 v[66:69], v[194:197], v[234:237], v[66:69]
	v_mfma_f32_16x16x32_bf16 v[58:61], v[198:201], v[234:237], v[58:61]
	v_mfma_f32_16x16x32_bf16 v[50:53], v[202:205], v[234:237], v[50:53]
	s_waitcnt lgkmcnt(0)
	s_barrier
	s_add_i32 s20, s20, 1
	s_add_i32 s18, s18, 2
	v_add_u32_e32 v182, s19, v191
	v_add_u32_e32 v238, s19, v192
	ds_read_b128 v[178:181], v182 offset:32768
	ds_read_b128 v[194:197], v182 offset:34816
	ds_read_b128 v[198:201], v182 offset:36864
	ds_read_b128 v[202:205], v182 offset:38912
	ds_read_b128 v[206:209], v238
	ds_read_b128 v[210:213], v238 offset:2048
	ds_read_b128 v[214:217], v238 offset:4096
	ds_read_b128 v[218:221], v238 offset:6144
	ds_read_b128 v[222:225], v238 offset:8192
	ds_read_b128 v[226:229], v238 offset:10240
	ds_read_b128 v[230:233], v238 offset:12288
	ds_read_b128 v[234:237], v238 offset:14336
	s_min_u32 s21, s20, 29
	s_xor_b32 s19, s19, 0x10000
	v_add_u32_e32 v239, s19, v189
	s_waitcnt lgkmcnt(0)
	s_add_i32 s21, s21, 2
	s_barrier
	v_mfma_f32_16x16x32_bf16 v[174:177], v[178:181], v[206:209], v[174:177]
	s_lshl_b32 s22, s21, 1
	s_and_b32 s22, s22, 0x60
	s_add_i32 s22, s22, s12
	s_lshl_b32 s22, s22, 6
	v_mfma_f32_16x16x32_bf16 v[170:173], v[194:197], v[206:209], v[170:173]
	s_and_b32 s22, s22, 0x3f00
	s_or_b32 s22, s22, s13
	s_lshl_b32 s23, s21, 23
	s_lshl_b32 s22, s22, 9
	v_mfma_f32_16x16x32_bf16 v[158:161], v[198:201], v[206:209], v[158:161]
	s_and_b32 s23, s23, 0x7000000
	s_or_b32 s22, s22, s23
	s_lshl_b32 s23, s21, 8
	s_and_b32 s23, s23, 0x100
	s_or_b32 s22, s22, s23
	s_or_b32 s23, s22, 0x4000
	v_mfma_f32_16x16x32_bf16 v[142:145], v[202:205], v[206:209], v[142:145]
	v_mfma_f32_16x16x32_bf16 v[166:169], v[178:181], v[210:213], v[166:169]
	v_mfma_f32_16x16x32_bf16 v[162:165], v[194:197], v[210:213], v[162:165]
	v_mfma_f32_16x16x32_bf16 v[146:149], v[198:201], v[210:213], v[146:149]
	s_or_b32 s23, s22, 0x8000
	v_mfma_f32_16x16x32_bf16 v[122:125], v[202:205], v[210:213], v[122:125]
	v_mfma_f32_16x16x32_bf16 v[154:157], v[178:181], v[214:217], v[154:157]
	v_mfma_f32_16x16x32_bf16 v[150:153], v[194:197], v[214:217], v[150:153]
	v_mfma_f32_16x16x32_bf16 v[130:133], v[198:201], v[214:217], v[130:133]
	s_or_b32 s23, s22, 0xc000
	v_mfma_f32_16x16x32_bf16 v[106:109], v[202:205], v[214:217], v[106:109]
	v_mfma_f32_16x16x32_bf16 v[138:141], v[178:181], v[218:221], v[138:141]
	v_mfma_f32_16x16x32_bf16 v[134:137], v[194:197], v[218:221], v[134:137]
	v_mfma_f32_16x16x32_bf16 v[114:117], v[198:201], v[218:221], v[114:117]
	s_or_b32 s23, s22, 0x10000
	v_mfma_f32_16x16x32_bf16 v[90:93], v[202:205], v[218:221], v[90:93]
	v_mfma_f32_16x16x32_bf16 v[126:129], v[178:181], v[222:225], v[126:129]
	v_mfma_f32_16x16x32_bf16 v[118:121], v[194:197], v[222:225], v[118:121]
	v_mfma_f32_16x16x32_bf16 v[98:101], v[198:201], v[222:225], v[98:101]
	s_or_b32 s23, s22, 0x14000
	v_mfma_f32_16x16x32_bf16 v[74:77], v[202:205], v[222:225], v[74:77]
	v_mfma_f32_16x16x32_bf16 v[110:113], v[178:181], v[226:229], v[110:113]
	v_mfma_f32_16x16x32_bf16 v[102:105], v[194:197], v[226:229], v[102:105]
	v_mfma_f32_16x16x32_bf16 v[82:85], v[198:201], v[226:229], v[82:85]
	s_or_b32 s23, s22, 0x18000
	s_or_b32 s22, s22, 0x1c000
	v_mfma_f32_16x16x32_bf16 v[62:65], v[202:205], v[226:229], v[62:65]
	v_mfma_f32_16x16x32_bf16 v[94:97], v[178:181], v[230:233], v[94:97]
	v_mfma_f32_16x16x32_bf16 v[86:89], v[194:197], v[230:233], v[86:89]
	v_mfma_f32_16x16x32_bf16 v[70:73], v[198:201], v[230:233], v[70:73]
	v_mfma_f32_16x16x32_bf16 v[54:57], v[202:205], v[230:233], v[54:57]
	v_mfma_f32_16x16x32_bf16 v[78:81], v[178:181], v[234:237], v[78:81]
	v_mfma_f32_16x16x32_bf16 v[66:69], v[194:197], v[234:237], v[66:69]
	v_mfma_f32_16x16x32_bf16 v[58:61], v[198:201], v[234:237], v[58:61]
	v_mfma_f32_16x16x32_bf16 v[50:53], v[202:205], v[234:237], v[50:53]
	s_waitcnt lgkmcnt(0)
	s_barrier
	ds_read_b128 v[178:181], v182 offset:33792
	ds_read_b128 v[194:197], v182 offset:35840
	ds_read_b128 v[198:201], v182 offset:37888
	ds_read_b128 v[202:205], v182 offset:39936
	ds_read_b128 v[206:209], v238 offset:1024
	ds_read_b128 v[210:213], v238 offset:3072
	ds_read_b128 v[214:217], v238 offset:5120
	ds_read_b128 v[218:221], v238 offset:7168
	ds_read_b128 v[222:225], v238 offset:9216
	ds_read_b128 v[226:229], v238 offset:11264
	ds_read_b128 v[230:233], v238 offset:13312
	ds_read_b128 v[234:237], v238 offset:15360
	s_waitcnt lgkmcnt(0)
	s_barrier
	v_mfma_f32_16x16x32_bf16 v[174:177], v[178:181], v[206:209], v[174:177]
	s_lshl_b32 s21, s21, 7
	s_and_b32 s21, s21, 0x780
	s_or_b32 s21, s21, s14
	s_or_b32 s22, s21, 0x20000
	v_mfma_f32_16x16x32_bf16 v[170:173], v[194:197], v[206:209], v[170:173]
	v_mfma_f32_16x16x32_bf16 v[158:161], v[198:201], v[206:209], v[158:161]
	v_mfma_f32_16x16x32_bf16 v[142:145], v[202:205], v[206:209], v[142:145]
	v_mfma_f32_16x16x32_bf16 v[166:169], v[178:181], v[210:213], v[166:169]
	v_mfma_f32_16x16x32_bf16 v[162:165], v[194:197], v[210:213], v[162:165]
	v_mfma_f32_16x16x32_bf16 v[146:149], v[198:201], v[210:213], v[146:149]
	v_mfma_f32_16x16x32_bf16 v[122:125], v[202:205], v[210:213], v[122:125]
	v_mfma_f32_16x16x32_bf16 v[154:157], v[178:181], v[214:217], v[154:157]
	v_mfma_f32_16x16x32_bf16 v[150:153], v[194:197], v[214:217], v[150:153]
	v_mfma_f32_16x16x32_bf16 v[130:133], v[198:201], v[214:217], v[130:133]
	v_mfma_f32_16x16x32_bf16 v[106:109], v[202:205], v[214:217], v[106:109]
	v_mfma_f32_16x16x32_bf16 v[138:141], v[178:181], v[218:221], v[138:141]
	v_mfma_f32_16x16x32_bf16 v[134:137], v[194:197], v[218:221], v[134:137]
	s_or_b32 s22, s21, 0x40000
	s_or_b32 s21, s21, 0x60000
	v_mfma_f32_16x16x32_bf16 v[114:117], v[198:201], v[218:221], v[114:117]
	v_mfma_f32_16x16x32_bf16 v[90:93], v[202:205], v[218:221], v[90:93]
	v_mfma_f32_16x16x32_bf16 v[126:129], v[178:181], v[222:225], v[126:129]
	v_mfma_f32_16x16x32_bf16 v[118:121], v[194:197], v[222:225], v[118:121]
	v_mfma_f32_16x16x32_bf16 v[98:101], v[198:201], v[222:225], v[98:101]
	v_mfma_f32_16x16x32_bf16 v[74:77], v[202:205], v[222:225], v[74:77]
	v_mfma_f32_16x16x32_bf16 v[110:113], v[178:181], v[226:229], v[110:113]
	v_mfma_f32_16x16x32_bf16 v[102:105], v[194:197], v[226:229], v[102:105]
	v_mfma_f32_16x16x32_bf16 v[82:85], v[198:201], v[226:229], v[82:85]
	v_mfma_f32_16x16x32_bf16 v[62:65], v[202:205], v[226:229], v[62:65]
	v_mfma_f32_16x16x32_bf16 v[94:97], v[178:181], v[230:233], v[94:97]
	v_mfma_f32_16x16x32_bf16 v[86:89], v[194:197], v[230:233], v[86:89]
	v_mfma_f32_16x16x32_bf16 v[70:73], v[198:201], v[230:233], v[70:73]
	v_mfma_f32_16x16x32_bf16 v[54:57], v[202:205], v[230:233], v[54:57]
	v_mfma_f32_16x16x32_bf16 v[78:81], v[178:181], v[234:237], v[78:81]
	v_mfma_f32_16x16x32_bf16 v[66:69], v[194:197], v[234:237], v[66:69]
	v_mfma_f32_16x16x32_bf16 v[58:61], v[198:201], v[234:237], v[58:61]
	v_mfma_f32_16x16x32_bf16 v[50:53], v[202:205], v[234:237], v[50:53]
	s_and_b32 s21, s18, 32
	s_add_i32 s21, s21, s12
	s_lshl_b32 s21, s21, 6
	s_and_b32 s21, s21, 0x3f00
	v_add_lshl_u32 v182, v193, s21, 9
	v_lshl_add_u64 v[206:207], v[184:185], 0, v[182:183]
	v_add_co_u32_e32 v208, vcc, s8, v206
	s_nop 1
	v_addc_co_u32_e32 v209, vcc, 0, v207, vcc
	v_add_co_u32_e32 v210, vcc, s15, v206
	s_nop 1
	v_addc_co_u32_e32 v211, vcc, 0, v207, vcc
	v_add_co_u32_e32 v212, vcc, s9, v206
	s_nop 1
	v_addc_co_u32_e32 v213, vcc, 0, v207, vcc
	v_add_co_u32_e32 v214, vcc, s16, v206
	s_nop 1
	v_addc_co_u32_e32 v215, vcc, 0, v207, vcc
	v_add_co_u32_e32 v216, vcc, s10, v206
	s_nop 1
	v_addc_co_u32_e32 v217, vcc, 0, v207, vcc
	v_add_co_u32_e32 v218, vcc, s17, v206
	s_nop 1
	v_addc_co_u32_e32 v219, vcc, 0, v207, vcc
	v_add_co_u32_e32 v220, vcc, s11, v206
	s_nop 1
	v_addc_co_u32_e32 v221, vcc, 0, v207, vcc
	global_store_dwordx4 v[206:207], v[174:177], off
	global_store_dwordx4 v[206:207], v[170:173], off offset:64
	global_store_dwordx4 v[206:207], v[158:161], off offset:128
	global_store_dwordx4 v[206:207], v[142:145], off offset:192
	global_store_dwordx4 v[208:209], v[166:169], off
	global_store_dwordx4 v[208:209], v[162:165], off offset:64
	global_store_dwordx4 v[208:209], v[146:149], off offset:128
	global_store_dwordx4 v[208:209], v[122:125], off offset:192
	global_store_dwordx4 v[210:211], v[154:157], off
	global_store_dwordx4 v[210:211], v[150:153], off offset:64
	global_store_dwordx4 v[210:211], v[130:133], off offset:128
	global_store_dwordx4 v[210:211], v[106:109], off offset:192
	global_store_dwordx4 v[212:213], v[138:141], off
	global_store_dwordx4 v[212:213], v[134:137], off offset:64
	global_store_dwordx4 v[212:213], v[114:117], off offset:128
	global_store_dwordx4 v[212:213], v[90:93], off offset:192
	global_store_dwordx4 v[214:215], v[126:129], off
	global_store_dwordx4 v[214:215], v[118:121], off offset:64
	global_store_dwordx4 v[214:215], v[98:101], off offset:128
	global_store_dwordx4 v[214:215], v[74:77], off offset:192
	global_store_dwordx4 v[216:217], v[110:113], off
	global_store_dwordx4 v[216:217], v[102:105], off offset:64
	global_store_dwordx4 v[216:217], v[82:85], off offset:128
	global_store_dwordx4 v[216:217], v[62:65], off offset:192
	global_store_dwordx4 v[218:219], v[94:97], off
	global_store_dwordx4 v[218:219], v[86:89], off offset:64
	global_store_dwordx4 v[218:219], v[70:73], off offset:128
	global_store_dwordx4 v[218:219], v[54:57], off offset:192
	global_store_dwordx4 v[220:221], v[78:81], off
	global_store_dwordx4 v[220:221], v[66:69], off offset:64
	global_store_dwordx4 v[220:221], v[58:61], off offset:128
	global_store_dwordx4 v[220:221], v[50:53], off offset:192
	s_waitcnt lgkmcnt(0)
	s_barrier
	s_branch .LBB1_6
.Lfirst:
	v_add_u32_e32 v182, s19, v191
	v_add_u32_e32 v238, s19, v192
	ds_read_b128 v[178:181], v182 offset:32768
	ds_read_b128 v[194:197], v182 offset:34816
	ds_read_b128 v[198:201], v182 offset:36864
	ds_read_b128 v[202:205], v182 offset:38912
	ds_read_b128 v[206:209], v238
	ds_read_b128 v[210:213], v238 offset:2048
	ds_read_b128 v[214:217], v238 offset:4096
	ds_read_b128 v[218:221], v238 offset:6144
	ds_read_b128 v[222:225], v238 offset:8192
	ds_read_b128 v[226:229], v238 offset:10240
	ds_read_b128 v[230:233], v238 offset:12288
	ds_read_b128 v[234:237], v238 offset:14336
	s_min_u32 s21, s20, 29
	s_xor_b32 s19, s19, 0x10000
	v_add_u32_e32 v239, s19, v189
	s_waitcnt vmcnt(11)
	v_cvt_pk_bf16_f32 v13, v12, v13
	v_cvt_pk_bf16_f32 v12, v10, v11
	s_waitcnt vmcnt(10)
	v_cvt_pk_bf16_f32 v11, v20, v21
	v_cvt_pk_bf16_f32 v10, v18, v19
	ds_write2st64_b64 v239, v[12:13], v[10:11] offset1:8
	s_waitcnt vmcnt(9)
	v_cvt_pk_bf16_f32 v11, v24, v25
	v_cvt_pk_bf16_f32 v10, v22, v23
	s_waitcnt vmcnt(8)
	v_cvt_pk_bf16_f32 v13, v32, v33
	v_cvt_pk_bf16_f32 v12, v30, v31
	ds_write2st64_b64 v239, v[10:11], v[12:13] offset0:16 offset1:24
	s_waitcnt vmcnt(7)
	v_cvt_pk_bf16_f32 v11, v36, v37
	v_cvt_pk_bf16_f32 v10, v34, v35
	s_waitcnt vmcnt(6)
	v_cvt_pk_bf16_f32 v13, v40, v41
	v_cvt_pk_bf16_f32 v12, v38, v39
	ds_write2st64_b64 v239, v[10:11], v[12:13] offset0:32 offset1:40
	s_waitcnt vmcnt(5)
	v_cvt_pk_bf16_f32 v11, v44, v45
	v_cvt_pk_bf16_f32 v10, v42, v43
	s_waitcnt vmcnt(4)
	v_cvt_pk_bf16_f32 v13, v48, v49
	v_cvt_pk_bf16_f32 v12, v46, v47
	ds_write2st64_b64 v239, v[10:11], v[12:13] offset0:48 offset1:56
	s_waitcnt lgkmcnt(0)
	s_add_i32 s21, s21, 2
	s_barrier
	v_mfma_f32_16x16x32_bf16 v[174:177], v[178:181], v[206:209], v[240:243]
	s_lshl_b32 s22, s21, 1
	s_and_b32 s22, s22, 0x60
	s_add_i32 s22, s22, s12
	s_lshl_b32 s22, s22, 6
	v_mfma_f32_16x16x32_bf16 v[170:173], v[194:197], v[206:209], v[244:247]
	s_and_b32 s22, s22, 0x3f00
	s_or_b32 s22, s22, s13
	s_lshl_b32 s23, s21, 23
	s_lshl_b32 s22, s22, 9
	v_mfma_f32_16x16x32_bf16 v[158:161], v[198:201], v[206:209], v[248:251]
	s_and_b32 s23, s23, 0x7000000
	s_or_b32 s22, s22, s23
	s_lshl_b32 s23, s21, 8
	s_and_b32 s23, s23, 0x100
	s_or_b32 s22, s22, s23
	s_or_b32 s23, s22, 0x4000
	buffer_load_dwordx4 v[10:13], v1, s[4:7], s22 offen sc0 nt
	v_mfma_f32_16x16x32_bf16 v[142:145], v[202:205], v[206:209], v[252:255]
	v_mfma_f32_16x16x32_bf16 v[166:169], v[178:181], v[210:213], v[240:243]
	v_mfma_f32_16x16x32_bf16 v[162:165], v[194:197], v[210:213], v[244:247]
	v_mfma_f32_16x16x32_bf16 v[146:149], v[198:201], v[210:213], v[248:251]
	buffer_load_dwordx4 v[18:21], v1, s[4:7], s23 offen sc0 nt
	s_or_b32 s23, s22, 0x8000
	v_mfma_f32_16x16x32_bf16 v[122:125], v[202:205], v[210:213], v[252:255]
	v_mfma_f32_16x16x32_bf16 v[154:157], v[178:181], v[214:217], v[240:243]
	v_mfma_f32_16x16x32_bf16 v[150:153], v[194:197], v[214:217], v[244:247]
	v_mfma_f32_16x16x32_bf16 v[130:133], v[198:201], v[214:217], v[248:251]
	buffer_load_dwordx4 v[22:25], v1, s[4:7], s23 offen sc0 nt
	s_or_b32 s23, s22, 0xc000
	v_mfma_f32_16x16x32_bf16 v[106:109], v[202:205], v[214:217], v[252:255]
	v_mfma_f32_16x16x32_bf16 v[138:141], v[178:181], v[218:221], v[240:243]
	v_mfma_f32_16x16x32_bf16 v[134:137], v[194:197], v[218:221], v[244:247]
	v_mfma_f32_16x16x32_bf16 v[114:117], v[198:201], v[218:221], v[248:251]
	buffer_load_dwordx4 v[30:33], v1, s[4:7], s23 offen sc0 nt
	s_or_b32 s23, s22, 0x10000
	v_mfma_f32_16x16x32_bf16 v[90:93], v[202:205], v[218:221], v[252:255]
	v_mfma_f32_16x16x32_bf16 v[126:129], v[178:181], v[222:225], v[240:243]
	v_mfma_f32_16x16x32_bf16 v[118:121], v[194:197], v[222:225], v[244:247]
	v_mfma_f32_16x16x32_bf16 v[98:101], v[198:201], v[222:225], v[248:251]
	buffer_load_dwordx4 v[34:37], v1, s[4:7], s23 offen sc0 nt
	s_or_b32 s23, s22, 0x14000
	v_mfma_f32_16x16x32_bf16 v[74:77], v[202:205], v[222:225], v[252:255]
	v_mfma_f32_16x16x32_bf16 v[110:113], v[178:181], v[226:229], v[240:243]
	v_mfma_f32_16x16x32_bf16 v[102:105], v[194:197], v[226:229], v[244:247]
	v_mfma_f32_16x16x32_bf16 v[82:85], v[198:201], v[226:229], v[248:251]
	buffer_load_dwordx4 v[38:41], v1, s[4:7], s23 offen sc0 nt
	s_or_b32 s23, s22, 0x18000
	s_or_b32 s22, s22, 0x1c000
	v_mfma_f32_16x16x32_bf16 v[62:65], v[202:205], v[226:229], v[252:255]
	v_mfma_f32_16x16x32_bf16 v[94:97], v[178:181], v[230:233], v[240:243]
	v_mfma_f32_16x16x32_bf16 v[86:89], v[194:197], v[230:233], v[244:247]
	v_mfma_f32_16x16x32_bf16 v[70:73], v[198:201], v[230:233], v[248:251]
	buffer_load_dwordx4 v[42:45], v1, s[4:7], s23 offen sc0 nt
	v_mfma_f32_16x16x32_bf16 v[54:57], v[202:205], v[230:233], v[252:255]
	v_mfma_f32_16x16x32_bf16 v[78:81], v[178:181], v[234:237], v[240:243]
	v_mfma_f32_16x16x32_bf16 v[66:69], v[194:197], v[234:237], v[244:247]
	v_mfma_f32_16x16x32_bf16 v[58:61], v[198:201], v[234:237], v[248:251]
	buffer_load_dwordx4 v[46:49], v1, s[4:7], s22 offen sc0 nt
	v_mfma_f32_16x16x32_bf16 v[50:53], v[202:205], v[234:237], v[252:255]
	s_waitcnt lgkmcnt(0)
	s_barrier
	ds_read_b128 v[178:181], v182 offset:33792
	ds_read_b128 v[194:197], v182 offset:35840
	ds_read_b128 v[198:201], v182 offset:37888
	ds_read_b128 v[202:205], v182 offset:39936
	ds_read_b128 v[206:209], v238 offset:1024
	ds_read_b128 v[210:213], v238 offset:3072
	ds_read_b128 v[214:217], v238 offset:5120
	ds_read_b128 v[218:221], v238 offset:7168
	ds_read_b128 v[222:225], v238 offset:9216
	ds_read_b128 v[226:229], v238 offset:11264
	ds_read_b128 v[230:233], v238 offset:13312
	ds_read_b128 v[234:237], v238 offset:15360
	v_add_u32_e32 v182, s19, v190
	s_waitcnt vmcnt(11)
	ds_write_b128 v182, v[2:5] offset:32768
	s_waitcnt vmcnt(10)
	ds_write_b128 v182, v[6:9] offset:40960
	s_waitcnt vmcnt(9)
	ds_write_b128 v182, v[14:17] offset:49152
	s_waitcnt vmcnt(8)
	ds_write_b128 v182, v[26:29] offset:57344
	s_waitcnt lgkmcnt(0)
	s_barrier
	v_mfma_f32_16x16x32_bf16 v[174:177], v[178:181], v[206:209], v[174:177]
	s_lshl_b32 s21, s21, 7
	s_and_b32 s21, s21, 0x780
	s_or_b32 s21, s21, s14
	s_or_b32 s22, s21, 0x20000
	v_mfma_f32_16x16x32_bf16 v[170:173], v[194:197], v[206:209], v[170:173]
	v_mfma_f32_16x16x32_bf16 v[158:161], v[198:201], v[206:209], v[158:161]
	v_mfma_f32_16x16x32_bf16 v[142:145], v[202:205], v[206:209], v[142:145]
	v_mfma_f32_16x16x32_bf16 v[166:169], v[178:181], v[210:213], v[166:169]
	v_mfma_f32_16x16x32_bf16 v[162:165], v[194:197], v[210:213], v[162:165]
	buffer_load_dwordx4 v[2:5], v188, s[0:3], s21 offen sc1
	v_mfma_f32_16x16x32_bf16 v[146:149], v[198:201], v[210:213], v[146:149]
	v_mfma_f32_16x16x32_bf16 v[122:125], v[202:205], v[210:213], v[122:125]
	v_mfma_f32_16x16x32_bf16 v[154:157], v[178:181], v[214:217], v[154:157]
	v_mfma_f32_16x16x32_bf16 v[150:153], v[194:197], v[214:217], v[150:153]
	v_mfma_f32_16x16x32_bf16 v[130:133], v[198:201], v[214:217], v[130:133]
	v_mfma_f32_16x16x32_bf16 v[106:109], v[202:205], v[214:217], v[106:109]
	v_mfma_f32_16x16x32_bf16 v[138:141], v[178:181], v[218:221], v[138:141]
	v_mfma_f32_16x16x32_bf16 v[134:137], v[194:197], v[218:221], v[134:137]
	buffer_load_dwordx4 v[6:9], v188, s[0:3], s22 offen sc1
	s_or_b32 s22, s21, 0x40000
	s_or_b32 s21, s21, 0x60000
	v_mfma_f32_16x16x32_bf16 v[114:117], v[198:201], v[218:221], v[114:117]
	v_mfma_f32_16x16x32_bf16 v[90:93], v[202:205], v[218:221], v[90:93]
	v_mfma_f32_16x16x32_bf16 v[126:129], v[178:181], v[222:225], v[126:129]
	v_mfma_f32_16x16x32_bf16 v[118:121], v[194:197], v[222:225], v[118:121]
	v_mfma_f32_16x16x32_bf16 v[98:101], v[198:201], v[222:225], v[98:101]
	v_mfma_f32_16x16x32_bf16 v[74:77], v[202:205], v[222:225], v[74:77]
	v_mfma_f32_16x16x32_bf16 v[110:113], v[178:181], v[226:229], v[110:113]
	v_mfma_f32_16x16x32_bf16 v[102:105], v[194:197], v[226:229], v[102:105]
	buffer_load_dwordx4 v[14:17], v188, s[0:3], s22 offen sc1
	v_mfma_f32_16x16x32_bf16 v[82:85], v[198:201], v[226:229], v[82:85]
	v_mfma_f32_16x16x32_bf16 v[62:65], v[202:205], v[226:229], v[62:65]
	v_mfma_f32_16x16x32_bf16 v[94:97], v[178:181], v[230:233], v[94:97]
	v_mfma_f32_16x16x32_bf16 v[86:89], v[194:197], v[230:233], v[86:89]
	v_mfma_f32_16x16x32_bf16 v[70:73], v[198:201], v[230:233], v[70:73]
	v_mfma_f32_16x16x32_bf16 v[54:57], v[202:205], v[230:233], v[54:57]
	v_mfma_f32_16x16x32_bf16 v[78:81], v[178:181], v[234:237], v[78:81]
	v_mfma_f32_16x16x32_bf16 v[66:69], v[194:197], v[234:237], v[66:69]
	buffer_load_dwordx4 v[26:29], v188, s[0:3], s21 offen sc1
	v_mfma_f32_16x16x32_bf16 v[58:61], v[198:201], v[234:237], v[58:61]
	v_mfma_f32_16x16x32_bf16 v[50:53], v[202:205], v[234:237], v[50:53]
	s_branch .LBB1_3
